# v45: v44 + second-half router weights: 9 of 16 row blocks prefetched into registers that the deeper logits read pipeline leaves free + static priority raise for waves 4-7 in the attention loop
# baseline (speedup 1.0000x reference)
; __device__ __forceinline__ void ph9_router(const Frame& F, const Args& A) {
;     ...
;     for (int grp = F.vcu; grp < S_ / 32; grp += F.G) {
;         int lane = F.lane; asm volatile("" : "+v"(lane));
;         const int tid = F.wave * 64 + lane;
;         const int r0 = grp * 32 + F.wave * 4;
;         if (tid < 32) cntL[tid] = 0u;
;         f32x4 hv[4][8];
;         { f32x4 t16[16];
; #pragma unroll
;           for (int i = 0; i < 16; ++i) t16[i] = ((const f32x4*)WRT)[tid + 512 * i];
;           __builtin_amdgcn_sched_barrier(0);
; #pragma unroll
;           for (int r = 0; r < 4; ++r) { const f32x4* xr = (const f32x4*)(X1 + (size_t)(r0 + r) * DM) + lane;
; #pragma unroll
;               for (int j = 0; j < 8; ++j) hv[r][j] = xr[64 * j]; }
;           __builtin_amdgcn_sched_barrier(0);
; #pragma unroll
;           for (int i = 0; i < 16; ++i) wl[tid + 512 * i] = t16[i]; }
.LBB0_1193:
	v_mov_b32_e32 v132, v1
	s_nop 0
	v_add_u32_e32 v134, s44, v132
	v_cmp_gt_i32_e64 s[2:3], 32, v134
	v_lshl_add_u32 v192, v134, 2, 0
	s_and_saveexec_b64 s[0:1], s[2:3]
	v_add_u32_e32 v2, 0x20500, v192
	ds_write_b32 v2, v131
	s_or_b64 exec, exec, s[0:1]
	v_ashrrev_i32_e32 v135, 31, v134
	v_lshl_add_u64 v[2:3], v[134:135], 4, s[20:21]
	v_add_co_u32_e32 v4, vcc, 0x2000, v2
	s_lshl_b32 s0, s52, 5
	s_nop 0
	v_addc_co_u32_e32 v5, vcc, 0, v3, vcc
	global_load_dwordx4 v[136:139], v[2:3], off
	global_load_dwordx4 v[140:143], v[4:5], off
	v_add_co_u32_e32 v4, vcc, 0x4000, v2
	s_add_i32 s40, s0, s45
	s_nop 0
	v_addc_co_u32_e32 v5, vcc, 0, v3, vcc
	v_add_co_u32_e32 v6, vcc, 0x6000, v2
	s_mov_b32 s42, 0
	s_nop 0
	v_addc_co_u32_e32 v7, vcc, 0, v3, vcc
	global_load_dwordx4 v[144:147], v[4:5], off
	global_load_dwordx4 v[148:151], v[6:7], off
	v_add_co_u32_e32 v4, vcc, 0x8000, v2
	s_nop 1
	v_addc_co_u32_e32 v5, vcc, 0, v3, vcc
	v_add_co_u32_e32 v6, vcc, 0xa000, v2
	s_nop 1
	v_addc_co_u32_e32 v7, vcc, 0, v3, vcc
	global_load_dwordx4 v[152:155], v[4:5], off
	global_load_dwordx4 v[156:159], v[6:7], off
	v_add_co_u32_e32 v4, vcc, 0xc000, v2
	s_nop 1
	v_addc_co_u32_e32 v5, vcc, 0, v3, vcc
	v_add_co_u32_e32 v6, vcc, 0xe000, v2
	s_nop 1
	v_addc_co_u32_e32 v7, vcc, 0, v3, vcc
	global_load_dwordx4 v[160:163], v[4:5], off
	global_load_dwordx4 v[164:167], v[6:7], off
	v_add_co_u32_e32 v4, vcc, 0x10000, v2
	s_nop 1
	v_addc_co_u32_e32 v5, vcc, 0, v3, vcc
	v_add_co_u32_e32 v6, vcc, 0x12000, v2
	s_nop 1
	v_addc_co_u32_e32 v7, vcc, 0, v3, vcc
	global_load_dwordx4 v[174:177], v[4:5], off
	global_load_dwordx4 v[194:197], v[6:7], off
	v_add_co_u32_e32 v4, vcc, 0x14000, v2
	s_nop 1
	v_addc_co_u32_e32 v5, vcc, 0, v3, vcc
	v_add_co_u32_e32 v6, vcc, 0x16000, v2
	s_nop 1
	v_addc_co_u32_e32 v7, vcc, 0, v3, vcc
	global_load_dwordx4 v[198:201], v[4:5], off
	global_load_dwordx4 v[202:205], v[6:7], off
	v_add_co_u32_e32 v4, vcc, 0x18000, v2
	s_nop 1
	v_addc_co_u32_e32 v5, vcc, 0, v3, vcc
	v_add_co_u32_e32 v6, vcc, 0x1a000, v2
	s_nop 1
	v_addc_co_u32_e32 v7, vcc, 0, v3, vcc
	global_load_dwordx4 v[206:209], v[4:5], off
	global_load_dwordx4 v[210:213], v[6:7], off
	v_add_co_u32_e32 v4, vcc, 0x1c000, v2
	s_nop 1
	v_addc_co_u32_e32 v5, vcc, 0, v3, vcc
	v_add_co_u32_e32 v2, vcc, 0x1e000, v2
	s_nop 1
	v_addc_co_u32_e32 v3, vcc, 0, v3, vcc
	global_load_dwordx4 v[214:217], v[4:5], off
	global_load_dwordx4 v[218:221], v[2:3], off
	v_readlane_b32 s4, v254, 33
	v_ashrrev_i32_e32 v133, 31, v132
	v_readlane_b32 s5, v254, 34
	s_ashr_i32 s41, s40, 31
	v_readlane_b32 s6, v254, 35
	v_lshl_add_u64 v[2:3], v[132:133], 4, s[4:5]
	s_lshl_b64 s[0:1], s[40:41], 13
	v_readlane_b32 s7, v254, 36
	v_lshl_add_u64 v[4:5], v[2:3], 0, s[0:1]
	s_or_b32 s6, s40, 1
	global_load_dwordx4 v[114:117], v[4:5], off
	global_load_dwordx4 v[102:105], v[4:5], off offset:1024
	global_load_dwordx4 v[94:97], v[4:5], off offset:2048
	global_load_dwordx4 v[90:93], v[4:5], off offset:3072
	v_add_co_u32_e32 v4, vcc, s46, v4
	s_ashr_i32 s7, s6, 31
	s_nop 0
	v_addc_co_u32_e32 v5, vcc, 0, v5, vcc
	s_lshl_b64 s[0:1], s[6:7], 13
	global_load_dwordx4 v[122:125], v[4:5], off
	global_load_dwordx4 v[118:121], v[4:5], off offset:1024
	global_load_dwordx4 v[106:109], v[4:5], off offset:2048
	global_load_dwordx4 v[98:101], v[4:5], off offset:3072
	v_lshl_add_u64 v[4:5], v[2:3], 0, s[0:1]
	s_or_b32 s4, s40, 2
	global_load_dwordx4 v[126:129], v[4:5], off
	global_load_dwordx4 v[110:113], v[4:5], off offset:1024
	global_load_dwordx4 v[86:89], v[4:5], off offset:2048
	global_load_dwordx4 v[82:85], v[4:5], off offset:3072
	v_add_co_u32_e32 v4, vcc, s46, v4
	s_ashr_i32 s5, s4, 31
	s_nop 0
	v_addc_co_u32_e32 v5, vcc, 0, v5, vcc
	s_lshl_b64 s[0:1], s[4:5], 13
	global_load_dwordx4 v[78:81], v[4:5], off
	global_load_dwordx4 v[74:77], v[4:5], off offset:1024
	global_load_dwordx4 v[70:73], v[4:5], off offset:2048
	global_load_dwordx4 v[62:65], v[4:5], off offset:3072
	v_lshl_add_u64 v[4:5], v[2:3], 0, s[0:1]
	s_or_b32 s0, s40, 3
	v_readlane_b32 s8, v254, 37
	v_readlane_b32 s9, v254, 38
	s_ashr_i32 s1, s0, 31
	global_load_dwordx4 v[66:69], v[4:5], off
	global_load_dwordx4 v[58:61], v[4:5], off offset:1024
	global_load_dwordx4 v[54:57], v[4:5], off offset:2048
	global_load_dwordx4 v[50:53], v[4:5], off offset:3072
	v_add_co_u32_e32 v4, vcc, s46, v4
	s_lshl_b64 s[8:9], s[0:1], 13
	s_nop 0
	v_addc_co_u32_e32 v5, vcc, 0, v5, vcc
	v_lshl_add_u64 v[2:3], v[2:3], 0, s[8:9]
	global_load_dwordx4 v[46:49], v[4:5], off
	global_load_dwordx4 v[42:45], v[4:5], off offset:1024
	global_load_dwordx4 v[38:41], v[4:5], off offset:2048
	global_load_dwordx4 v[34:37], v[4:5], off offset:3072
	global_load_dwordx4 v[30:33], v[2:3], off
	global_load_dwordx4 v[26:29], v[2:3], off offset:1024
	global_load_dwordx4 v[22:25], v[2:3], off offset:2048
	global_load_dwordx4 v[18:21], v[2:3], off offset:3072
	v_add_co_u32_e32 v2, vcc, s46, v2
	v_readlane_b32 s10, v254, 39
	s_nop 0
	v_addc_co_u32_e32 v3, vcc, 0, v3, vcc
	global_load_dwordx4 v[14:17], v[2:3], off
	global_load_dwordx4 v[10:13], v[2:3], off offset:1024
	global_load_dwordx4 v[6:9], v[2:3], off offset:2048
	s_nop 0
	global_load_dwordx4 v[2:5], v[2:3], off offset:3072
	v_readlane_b32 s11, v254, 40
	v_readlane_b32 s12, v254, 41
	v_readlane_b32 s13, v254, 42
	v_readlane_b32 s14, v254, 43
	v_readlane_b32 s15, v254, 44
	v_readlane_b32 s16, v254, 45
	v_readlane_b32 s17, v254, 46
	v_readlane_b32 s18, v254, 47
	v_readlane_b32 s19, v254, 48
	v_lshl_add_u32 v135, v134, 4, 0
	v_add_u32_e32 v130, 0x10000, v135
	s_waitcnt vmcnt(47)
	ds_write_b128 v135, v[136:139]
	s_waitcnt vmcnt(46)
	ds_write_b128 v135, v[140:143] offset:8192
	s_waitcnt vmcnt(45)
; __device__ __forceinline__ void ph9_router(const Frame& F, const Args& A) {
;     ...
;           for (int i = 0; i < 16; ++i) wl[tid + 512 * i] = t16[i]; }
;         __builtin_amdgcn_sched_barrier(0);
; #pragma unroll
;         for (int r = 0; r < 4; ++r) { const uint2* dr = (const uint2*)(DX + (size_t)(r0 + r) * DM) + lane; uint2 dw[8];
; #pragma unroll
;             for (int j = 0; j < 8; ++j) dw[j] = dr[64 * j];
; #pragma unroll
;             for (int j = 0; j < 8; ++j) { hv[r][j].x += bflo(dw[j].x); hv[r][j].y += bfhi(dw[j].x); hv[r][j].z += bflo(dw[j].y); hv[r][j].w += bfhi(dw[j].y); } }
	ds_write_b128 v135, v[144:147] offset:16384
	s_waitcnt vmcnt(44)
	ds_write_b128 v135, v[148:151] offset:24576
	s_waitcnt vmcnt(43)
	ds_write_b128 v135, v[152:155] offset:32768
	s_waitcnt vmcnt(42)
	ds_write_b128 v135, v[156:159] offset:40960
	s_waitcnt vmcnt(41)
	ds_write_b128 v135, v[160:163] offset:49152
	s_waitcnt vmcnt(40)
	ds_write_b128 v135, v[164:167] offset:57344
	s_waitcnt vmcnt(39)
	ds_write_b128 v130, v[174:177]
	v_add_u32_e32 v130, 0x12000, v135
	s_waitcnt vmcnt(38)
	ds_write_b128 v130, v[194:197]
	v_add_u32_e32 v130, 0x14000, v135
	s_waitcnt vmcnt(37)
	ds_write_b128 v130, v[198:201]
	v_add_u32_e32 v130, 0x16000, v135
	s_waitcnt vmcnt(36)
	ds_write_b128 v130, v[202:205]
	v_add_u32_e32 v130, 0x18000, v135
	s_waitcnt vmcnt(35)
	ds_write_b128 v130, v[206:209]
	v_add_u32_e32 v130, 0x1a000, v135
	s_waitcnt vmcnt(34)
	ds_write_b128 v130, v[210:213]
	v_add_u32_e32 v130, 0x1c000, v135
	s_waitcnt vmcnt(33)
	ds_write_b128 v130, v[214:217]
	v_add_u32_e32 v130, 0x1e000, v135
	s_waitcnt vmcnt(32)
	ds_write_b128 v130, v[218:221]
	v_lshl_add_u64 v[136:137], v[132:133], 3, s[58:59]
	s_lshl_b64 s[8:9], s[40:41], 12
	v_lshl_add_u64 v[138:139], v[136:137], 0, s[8:9]
	global_load_dwordx2 v[140:141], v[138:139], off
	global_load_dwordx2 v[142:143], v[138:139], off offset:512
	global_load_dwordx2 v[144:145], v[138:139], off offset:1024
	global_load_dwordx2 v[146:147], v[138:139], off offset:1536
	global_load_dwordx2 v[148:149], v[138:139], off offset:2048
	global_load_dwordx2 v[150:151], v[138:139], off offset:2560
	global_load_dwordx2 v[152:153], v[138:139], off offset:3072
	s_nop 0
	global_load_dwordx2 v[138:139], v[138:139], off offset:3584
	s_lshl_b64 s[6:7], s[6:7], 12
	v_lshl_add_u64 v[154:155], v[136:137], 0, s[6:7]
	global_load_dwordx2 v[156:157], v[154:155], off
	global_load_dwordx2 v[164:165], v[154:155], off offset:512
	global_load_dwordx2 v[166:167], v[154:155], off offset:1024
	global_load_dwordx2 v[174:175], v[154:155], off offset:1536
	s_lshl_b64 s[4:5], s[4:5], 12
	v_lshl_add_u64 v[176:177], v[136:137], 0, s[4:5]
	global_load_dwordx2 v[178:179], v[154:155], off offset:2048
	global_load_dwordx2 v[194:195], v[154:155], off offset:2560
	global_load_dwordx2 v[196:197], v[154:155], off offset:3072
	global_load_dwordx2 v[198:199], v[154:155], off offset:3584
	global_load_dwordx2 v[200:201], v[176:177], off
	global_load_dwordx2 v[202:203], v[176:177], off offset:512
	global_load_dwordx2 v[204:205], v[176:177], off offset:1024
	global_load_dwordx2 v[206:207], v[176:177], off offset:1536
	global_load_dwordx2 v[208:209], v[176:177], off offset:2048
	s_lshl_b64 s[0:1], s[0:1], 12
	v_cmp_lt_i32_e32 vcc, v182, v181
	s_waitcnt vmcnt(20)
	v_lshlrev_b32_e32 v154, 16, v140
	s_waitcnt vmcnt(19)
	v_lshlrev_b32_e32 v160, 16, v142
	v_and_b32_e32 v161, 0xffff0000, v142
	v_lshlrev_b32_e32 v142, 16, v143
	v_and_b32_e32 v143, 0xffff0000, v143
	s_waitcnt vmcnt(17)
	v_lshlrev_b32_e32 v210, 16, v146
	v_and_b32_e32 v211, 0xffff0000, v146
	s_waitcnt vmcnt(15)
	v_lshlrev_b32_e32 v218, 16, v150
	v_and_b32_e32 v219, 0xffff0000, v150
	v_lshlrev_b32_e32 v214, 16, v148
	v_and_b32_e32 v215, 0xffff0000, v148
	v_lshlrev_b32_e32 v216, 16, v149
	v_and_b32_e32 v217, 0xffff0000, v149
	v_pk_add_f32 v[148:149], v[104:105], v[142:143]
	v_pk_add_f32 v[104:105], v[90:91], v[210:211]
	v_pk_add_f32 v[90:91], v[118:119], v[218:219]
	global_load_dwordx2 v[118:119], v[176:177], off offset:2560
	v_and_b32_e32 v155, 0xffff0000, v140
	v_lshlrev_b32_e32 v140, 16, v141
	v_and_b32_e32 v141, 0xffff0000, v141
	v_lshlrev_b32_e32 v212, 16, v147
	v_and_b32_e32 v213, 0xffff0000, v147
	v_lshlrev_b32_e32 v150, 16, v151
	v_and_b32_e32 v151, 0xffff0000, v151
	v_pk_add_f32 v[158:159], v[116:117], v[140:141]
	v_pk_add_f32 v[116:117], v[92:93], v[212:213]
	v_pk_add_f32 v[92:93], v[120:121], v[150:151]
	global_load_dwordx2 v[120:121], v[176:177], off offset:3072
	s_waitcnt vmcnt(15)
	v_lshlrev_b32_e32 v222, 16, v138
	v_and_b32_e32 v223, 0xffff0000, v138
	s_waitcnt vmcnt(14)
	v_lshlrev_b32_e32 v224, 16, v156
	v_and_b32_e32 v225, 0xffff0000, v156
	v_lshlrev_b32_e32 v226, 16, v157
	v_and_b32_e32 v227, 0xffff0000, v157
	v_pk_add_f32 v[156:157], v[114:115], v[154:155]
	v_pk_add_f32 v[114:115], v[98:99], v[222:223]
	s_waitcnt vmcnt(13)
	v_lshlrev_b32_e32 v98, 16, v165
	v_and_b32_e32 v99, 0xffff0000, v165
	v_lshlrev_b32_e32 v162, 16, v144
	v_and_b32_e32 v163, 0xffff0000, v144
	v_lshlrev_b32_e32 v144, 16, v145
	v_and_b32_e32 v145, 0xffff0000, v145
	v_lshlrev_b32_e32 v138, 16, v139
	v_and_b32_e32 v139, 0xffff0000, v139
	v_pk_add_f32 v[154:155], v[112:113], v[98:99]
	s_waitcnt vmcnt(12)
	v_lshlrev_b32_e32 v98, 16, v166
	v_and_b32_e32 v99, 0xffff0000, v166
	v_lshlrev_b32_e32 v220, 16, v152
	v_and_b32_e32 v221, 0xffff0000, v152
	v_lshlrev_b32_e32 v152, 16, v153
	v_and_b32_e32 v153, 0xffff0000, v153
	v_pk_add_f32 v[140:141], v[94:95], v[162:163]
	v_pk_add_f32 v[142:143], v[96:97], v[144:145]
	v_pk_add_f32 v[96:97], v[122:123], v[214:215]
	v_pk_add_f32 v[122:123], v[100:101], v[138:139]
	v_pk_add_f32 v[162:163], v[128:129], v[226:227]
	v_pk_add_f32 v[128:129], v[86:87], v[98:99]
	v_lshlrev_b32_e32 v86, 16, v167
	v_and_b32_e32 v87, 0xffff0000, v167
	global_load_dwordx2 v[138:139], v[176:177], off offset:3584
	v_pk_add_f32 v[94:95], v[106:107], v[220:221]
	v_pk_add_f32 v[106:107], v[108:109], v[152:153]
	v_pk_add_f32 v[144:145], v[88:89], v[86:87]
	s_waitcnt vmcnt(12)
	v_lshlrev_b32_e32 v86, 16, v174
	v_and_b32_e32 v87, 0xffff0000, v174
	v_lshl_add_u64 v[152:153], v[136:137], 0, s[0:1]
	v_lshlrev_b32_e32 v228, 16, v164
	v_and_b32_e32 v229, 0xffff0000, v164
	v_pk_add_f32 v[86:87], v[82:83], v[86:87]
	v_lshlrev_b32_e32 v82, 16, v175
	v_and_b32_e32 v83, 0xffff0000, v175
	global_load_dwordx2 v[164:165], v[152:153], off
	global_load_dwordx2 v[166:167], v[152:153], off offset:512
	v_pk_add_f32 v[88:89], v[84:85], v[82:83]
	s_waitcnt vmcnt(13)
; __device__ __forceinline__ void ph9_router(const Frame& F, const Args& A) {
;     ...
;         for (int r = 0; r < 4; ++r) { const uint2* dr = (const uint2*)(DX + (size_t)(r0 + r) * DM) + lane; uint2 dw[8];
; #pragma unroll
;             for (int j = 0; j < 8; ++j) dw[j] = dr[64 * j];
; #pragma unroll
;             for (int j = 0; j < 8; ++j) { hv[r][j].x += bflo(dw[j].x); hv[r][j].y += bfhi(dw[j].x); hv[r][j].z += bflo(dw[j].y); hv[r][j].w += bfhi(dw[j].y); } }
	v_lshlrev_b32_e32 v82, 16, v178
	v_and_b32_e32 v83, 0xffff0000, v178
	v_pk_add_f32 v[78:79], v[78:79], v[82:83]
	v_lshlrev_b32_e32 v82, 16, v179
	v_and_b32_e32 v83, 0xffff0000, v179
	v_pk_add_f32 v[100:101], v[80:81], v[82:83]
	s_waitcnt vmcnt(12)
	v_lshlrev_b32_e32 v80, 16, v194
	v_and_b32_e32 v81, 0xffff0000, v194
	v_pk_add_f32 v[82:83], v[74:75], v[80:81]
	v_lshlrev_b32_e32 v74, 16, v195
	global_load_dwordx2 v[80:81], v[152:153], off offset:1024
	v_and_b32_e32 v75, 0xffff0000, v195
	v_pk_add_f32 v[84:85], v[76:77], v[74:75]
	s_waitcnt vmcnt(12)
	v_lshlrev_b32_e32 v74, 16, v196
	v_and_b32_e32 v75, 0xffff0000, v196
	v_pk_add_f32 v[98:99], v[70:71], v[74:75]
	global_load_dwordx2 v[74:75], v[152:153], off offset:1536
	global_load_dwordx2 v[76:77], v[152:153], off offset:2048
	global_load_dwordx2 v[174:175], v[152:153], off offset:2560
	v_lshlrev_b32_e32 v70, 16, v197
	v_and_b32_e32 v71, 0xffff0000, v197
	v_pk_add_f32 v[108:109], v[72:73], v[70:71]
	s_waitcnt vmcnt(14)
	v_lshlrev_b32_e32 v70, 16, v198
	v_and_b32_e32 v71, 0xffff0000, v198
	v_pk_add_f32 v[150:151], v[110:111], v[228:229]
	v_pk_add_f32 v[110:111], v[62:63], v[70:71]
	v_lshlrev_b32_e32 v62, 16, v199
	v_and_b32_e32 v63, 0xffff0000, v199
	v_pk_add_f32 v[146:147], v[102:103], v[160:161]
	v_pk_add_f32 v[102:103], v[124:125], v[216:217]
	v_pk_add_f32 v[124:125], v[64:65], v[62:63]
	s_waitcnt vmcnt(13)
	v_lshlrev_b32_e32 v62, 16, v200
	v_and_b32_e32 v63, 0xffff0000, v200
	v_pk_add_f32 v[72:73], v[66:67], v[62:63]
	v_lshlrev_b32_e32 v62, 16, v201
	v_and_b32_e32 v63, 0xffff0000, v201
	v_pk_add_f32 v[68:69], v[68:69], v[62:63]
	s_waitcnt vmcnt(12)
	v_lshlrev_b32_e32 v62, 16, v202
	v_and_b32_e32 v63, 0xffff0000, v202
	v_pk_add_f32 v[62:63], v[58:59], v[62:63]
	v_lshlrev_b32_e32 v58, 16, v203
	v_and_b32_e32 v59, 0xffff0000, v203
	v_pk_add_f32 v[64:65], v[60:61], v[58:59]
	s_waitcnt vmcnt(11)
	v_lshlrev_b32_e32 v58, 16, v204
	v_and_b32_e32 v59, 0xffff0000, v204
	v_pk_add_f32 v[54:55], v[54:55], v[58:59]
	v_lshlrev_b32_e32 v58, 16, v205
	v_and_b32_e32 v59, 0xffff0000, v205
	v_pk_add_f32 v[56:57], v[56:57], v[58:59]
	s_waitcnt vmcnt(10)
	v_lshlrev_b32_e32 v58, 16, v206
	v_and_b32_e32 v59, 0xffff0000, v206
	v_pk_add_f32 v[50:51], v[50:51], v[58:59]
	v_lshlrev_b32_e32 v58, 16, v207
	v_and_b32_e32 v59, 0xffff0000, v207
	v_pk_add_f32 v[58:59], v[52:53], v[58:59]
	s_waitcnt vmcnt(9)
	v_lshlrev_b32_e32 v52, 16, v208
	v_and_b32_e32 v53, 0xffff0000, v208
	v_pk_add_f32 v[66:67], v[46:47], v[52:53]
	v_lshlrev_b32_e32 v46, 16, v209
	v_and_b32_e32 v47, 0xffff0000, v209
	v_pk_add_f32 v[70:71], v[48:49], v[46:47]
	s_waitcnt vmcnt(8)
	v_lshlrev_b32_e32 v46, 16, v118
	v_and_b32_e32 v47, 0xffff0000, v118
	v_pk_add_f32 v[112:113], v[42:43], v[46:47]
	v_lshlrev_b32_e32 v42, 16, v119
	v_and_b32_e32 v43, 0xffff0000, v119
	v_pk_add_f32 v[160:161], v[126:127], v[224:225]
	v_pk_add_f32 v[126:127], v[44:45], v[42:43]
	s_waitcnt vmcnt(7)
	v_lshlrev_b32_e32 v42, 16, v120
	v_and_b32_e32 v43, 0xffff0000, v120
	v_pk_add_f32 v[118:119], v[38:39], v[42:43]
	global_load_dwordx2 v[44:45], v[152:153], off offset:3072
	global_load_dwordx2 v[42:43], v[152:153], off offset:3584
	v_lshlrev_b32_e32 v38, 16, v121
	v_and_b32_e32 v39, 0xffff0000, v121
	v_pk_add_f32 v[120:121], v[40:41], v[38:39]
	s_waitcnt vmcnt(8)
	v_lshlrev_b32_e32 v38, 16, v138
	v_and_b32_e32 v39, 0xffff0000, v138
	v_pk_add_f32 v[136:137], v[34:35], v[38:39]
	v_lshlrev_b32_e32 v34, 16, v139
	v_and_b32_e32 v35, 0xffff0000, v139
	v_pk_add_f32 v[138:139], v[36:37], v[34:35]
	s_waitcnt vmcnt(7)
	v_lshlrev_b32_e32 v34, 16, v164
	v_and_b32_e32 v35, 0xffff0000, v164
	v_pk_add_f32 v[38:39], v[30:31], v[34:35]
	v_lshlrev_b32_e32 v30, 16, v165
	v_and_b32_e32 v31, 0xffff0000, v165
	v_pk_add_f32 v[40:41], v[32:33], v[30:31]
	s_waitcnt vmcnt(6)
	v_lshlrev_b32_e32 v30, 16, v166
	v_and_b32_e32 v31, 0xffff0000, v166
	v_pk_add_f32 v[32:33], v[26:27], v[30:31]
	v_lshlrev_b32_e32 v26, 16, v167
	v_and_b32_e32 v27, 0xffff0000, v167
	v_pk_add_f32 v[28:29], v[28:29], v[26:27]
	s_waitcnt vmcnt(5)
	v_lshlrev_b32_e32 v26, 16, v80
	v_and_b32_e32 v27, 0xffff0000, v80
	v_pk_add_f32 v[34:35], v[22:23], v[26:27]
	v_lshlrev_b32_e32 v22, 16, v81
	v_and_b32_e32 v23, 0xffff0000, v81
	v_pk_add_f32 v[36:37], v[24:25], v[22:23]
	s_waitcnt vmcnt(4)
	v_lshlrev_b32_e32 v22, 16, v74
	v_and_b32_e32 v23, 0xffff0000, v74
	v_pk_add_f32 v[46:47], v[18:19], v[22:23]
	v_lshlrev_b32_e32 v18, 16, v75
	v_and_b32_e32 v19, 0xffff0000, v75
	v_pk_add_f32 v[60:61], v[20:21], v[18:19]
	s_waitcnt vmcnt(3)
	v_lshlrev_b32_e32 v18, 16, v76
	v_and_b32_e32 v19, 0xffff0000, v76
	v_pk_add_f32 v[74:75], v[14:15], v[18:19]
	v_lshlrev_b32_e32 v14, 16, v77
	v_and_b32_e32 v15, 0xffff0000, v77
	v_pk_add_f32 v[164:165], v[16:17], v[14:15]
	s_waitcnt vmcnt(2)
; __device__ __forceinline__ void ph9_router(const Frame& F, const Args& A) {
;     ...
;         for (int r = 0; r < 4; ++r) { const uint2* dr = (const uint2*)(DX + (size_t)(r0 + r) * DM) + lane; uint2 dw[8];
; #pragma unroll
;             for (int j = 0; j < 8; ++j) dw[j] = dr[64 * j];
; #pragma unroll
;             for (int j = 0; j < 8; ++j) { hv[r][j].x += bflo(dw[j].x); hv[r][j].y += bfhi(dw[j].x); hv[r][j].z += bflo(dw[j].y); hv[r][j].w += bfhi(dw[j].y); } }
;         float rstd[4];
; #pragma unroll
;         for (int r = 0; r < 4; ++r) { float ss = 0.f;
; #pragma unroll
;             for (int j = 0; j < 8; ++j) ss += (hv[r][j].x * hv[r][j].x + hv[r][j].y * hv[r][j].y) + (hv[r][j].z * hv[r][j].z + hv[r][j].w * hv[r][j].w);
;             rstd[r] = 1.f / sqrtf(wave_sum(ss) * (1.f / DM) + EPS_); }
	v_lshlrev_b32_e32 v14, 16, v174
	v_and_b32_e32 v15, 0xffff0000, v174
	v_pk_add_f32 v[152:153], v[10:11], v[14:15]
	v_cndmask_b32_e32 v14, v180, v182, vcc
	v_mov_b32_e32 v16, v157
	v_mov_b32_e32 v17, v147
	v_lshlrev_b32_e32 v193, 2, v14
	v_mov_b32_e32 v14, v156
	v_mov_b32_e32 v15, v146
	v_pk_mul_f32 v[16:17], v[16:17], v[16:17]
	v_mov_b32_e32 v18, v159
	v_mov_b32_e32 v19, v149
	v_pk_fma_f32 v[14:15], v[14:15], v[14:15], v[16:17]
	v_mov_b32_e32 v16, v158
	v_mov_b32_e32 v17, v148
	v_pk_mul_f32 v[18:19], v[18:19], v[18:19]
	v_mul_f32_e32 v20, v117, v117
	v_pk_fma_f32 v[16:17], v[16:17], v[16:17], v[18:19]
	v_mov_b32_e32 v18, v141
	v_mov_b32_e32 v19, v143
	v_pk_add_f32 v[14:15], v[14:15], v[16:17]
	v_mov_b32_e32 v16, v140
	v_mov_b32_e32 v17, v142
	v_pk_mul_f32 v[18:19], v[18:19], v[18:19]
	v_pk_add_f32 v[14:15], v[14:15], v[14:15] op_sel:[0,1] op_sel_hi:[1,0]
	v_pk_fma_f32 v[16:17], v[16:17], v[16:17], v[18:19]
	v_mul_f32_e32 v18, v105, v105
	v_pk_add_f32 v[16:17], v[16:17], v[16:17] op_sel:[0,1] op_sel_hi:[1,0]
	v_pk_fma_f32 v[18:19], v[104:105], v[104:105], v[18:19] op_sel_hi:[1,1,0]
	v_pk_fma_f32 v[20:21], v[116:117], v[116:117], v[20:21] op_sel_hi:[1,1,0]
	v_pk_mul_f32 v[22:23], v[96:97], v[96:97]
	v_pk_mul_f32 v[24:25], v[102:103], v[102:103]
	v_mov_b32_e32 v15, v22
	v_mov_b32_e32 v17, v23
	v_mov_b32_e32 v19, v24
	v_mov_b32_e32 v21, v25
	v_pk_add_f32 v[14:15], v[14:15], v[16:17]
	v_pk_add_f32 v[16:17], v[18:19], v[20:21]
	v_mov_b32_e32 v18, v91
	v_mov_b32_e32 v19, v93
	v_pk_add_f32 v[14:15], v[14:15], v[16:17]
	v_mov_b32_e32 v16, v90
	v_mov_b32_e32 v17, v92
	v_pk_mul_f32 v[18:19], v[18:19], v[18:19]
	v_mul_f32_e32 v20, v107, v107
	v_pk_fma_f32 v[16:17], v[16:17], v[16:17], v[18:19]
	v_mul_f32_e32 v18, v95, v95
	v_pk_add_f32 v[14:15], v[14:15], v[14:15] op_sel:[0,1] op_sel_hi:[1,0]
	v_pk_add_f32 v[16:17], v[16:17], v[16:17] op_sel:[0,1] op_sel_hi:[1,0]
	v_pk_fma_f32 v[18:19], v[94:95], v[94:95], v[18:19] op_sel_hi:[1,1,0]
	v_pk_fma_f32 v[20:21], v[106:107], v[106:107], v[20:21] op_sel_hi:[1,1,0]
	v_pk_mul_f32 v[22:23], v[114:115], v[114:115]
	v_pk_mul_f32 v[24:25], v[122:123], v[122:123]
	v_mov_b32_e32 v15, v22
	v_mov_b32_e32 v17, v23
	v_mov_b32_e32 v19, v24
	v_mov_b32_e32 v21, v25
	v_pk_add_f32 v[14:15], v[14:15], v[16:17]
	v_pk_add_f32 v[16:17], v[18:19], v[20:21]
	v_lshlrev_b32_e32 v10, 16, v175
	v_pk_add_f32 v[14:15], v[14:15], v[16:17]
	v_and_b32_e32 v11, 0xffff0000, v175
	v_add_f32_e32 v14, v14, v15
	ds_bpermute_b32 v15, v193, v14
	v_cmp_lt_i32_e32 vcc, v183, v181
	v_pk_add_f32 v[166:167], v[12:13], v[10:11]
	v_mov_b32_e32 v16, v163
	v_cndmask_b32_e32 v10, v180, v183, vcc
	v_lshlrev_b32_e32 v196, 2, v10
	s_waitcnt lgkmcnt(0)
	v_add_f32_e32 v11, v14, v15
	ds_bpermute_b32 v12, v196, v11
	v_cmp_lt_i32_e32 vcc, v184, v181
	s_waitcnt vmcnt(1)
	v_lshlrev_b32_e32 v10, 16, v44
	v_mov_b32_e32 v15, v151
	v_cndmask_b32_e32 v13, v180, v184, vcc
	v_lshlrev_b32_e32 v195, 2, v13
	s_waitcnt lgkmcnt(0)
	v_add_f32_e32 v12, v11, v12
	ds_bpermute_b32 v13, v195, v12
	v_cmp_lt_i32_e32 vcc, v185, v181
	v_and_b32_e32 v11, 0xffff0000, v44
	v_pk_add_f32 v[6:7], v[6:7], v[10:11]
	v_cndmask_b32_e32 v14, v180, v185, vcc
	v_lshlrev_b32_e32 v194, 2, v14
	s_waitcnt lgkmcnt(0)
	v_add_f32_e32 v12, v12, v13
	ds_bpermute_b32 v13, v194, v12
	v_cmp_lt_i32_e32 vcc, v186, v181
	v_mov_b32_e32 v14, v161
	v_pk_mul_f32 v[14:15], v[14:15], v[14:15]
	v_cndmask_b32_e32 v10, v180, v186, vcc
	v_lshlrev_b32_e32 v197, 2, v10
	s_waitcnt lgkmcnt(0)
	v_add_f32_e32 v11, v12, v13
	ds_bpermute_b32 v12, v197, v11
	v_cmp_lt_i32_e32 vcc, v187, v181
	v_mov_b32_e32 v17, v155
	v_pk_mul_f32 v[16:17], v[16:17], v[16:17]
	v_cndmask_b32_e32 v13, v180, v187, vcc
	v_lshlrev_b32_e32 v198, 2, v13
	s_waitcnt lgkmcnt(0)
	v_add_f32_e32 v12, v11, v12
	ds_bpermute_b32 v13, v198, v12
	v_mul_f32_e32 v18, v89, v89
	v_pk_fma_f32 v[18:19], v[88:89], v[88:89], v[18:19] op_sel_hi:[1,1,0]
	v_pk_mul_f32 v[20:21], v[78:79], v[78:79]
	v_pk_mul_f32 v[22:23], v[100:101], v[100:101]
	s_waitcnt lgkmcnt(0)
	v_add_f32_e32 v12, v12, v13
	v_fmamk_f32 v12, v12, 0x3a000000, v169
	v_mul_f32_e32 v13, 0x4f800000, v12
	v_cmp_gt_f32_e32 vcc, s47, v12
	v_mov_b32_e32 v19, v23
	v_lshlrev_b32_e32 v10, 16, v45
	v_cndmask_b32_e32 v24, v12, v13, vcc
	v_mov_b32_e32 v12, v160
	v_mov_b32_e32 v13, v150
	v_pk_fma_f32 v[12:13], v[12:13], v[12:13], v[14:15]
	v_mov_b32_e32 v14, v162
	v_mov_b32_e32 v15, v154
	v_pk_fma_f32 v[14:15], v[14:15], v[14:15], v[16:17]
	v_mov_b32_e32 v16, v129
	v_mov_b32_e32 v17, v145
	v_pk_add_f32 v[12:13], v[12:13], v[14:15]
	v_mov_b32_e32 v14, v128
	v_mov_b32_e32 v15, v144
	v_pk_mul_f32 v[16:17], v[16:17], v[16:17]
	v_pk_add_f32 v[12:13], v[12:13], v[12:13] op_sel:[0,1] op_sel_hi:[1,0]
	v_pk_fma_f32 v[14:15], v[14:15], v[14:15], v[16:17]
	v_mul_f32_e32 v16, v87, v87
	v_pk_add_f32 v[14:15], v[14:15], v[14:15] op_sel:[0,1] op_sel_hi:[1,0]
	v_pk_fma_f32 v[16:17], v[86:87], v[86:87], v[16:17] op_sel_hi:[1,1,0]
	v_mov_b32_e32 v13, v20
	v_mov_b32_e32 v15, v21
	v_mov_b32_e32 v17, v22
	v_pk_add_f32 v[12:13], v[12:13], v[14:15]
	v_pk_add_f32 v[14:15], v[16:17], v[18:19]
	v_mov_b32_e32 v16, v83
	v_mov_b32_e32 v17, v85
	v_pk_add_f32 v[12:13], v[12:13], v[14:15]
	v_mov_b32_e32 v14, v82
	v_mov_b32_e32 v15, v84
	v_pk_mul_f32 v[16:17], v[16:17], v[16:17]
	v_mul_f32_e32 v18, v109, v109
	v_pk_fma_f32 v[14:15], v[14:15], v[14:15], v[16:17]
	v_mul_f32_e32 v16, v99, v99
	v_pk_add_f32 v[12:13], v[12:13], v[12:13] op_sel:[0,1] op_sel_hi:[1,0]
	v_pk_add_f32 v[14:15], v[14:15], v[14:15] op_sel:[0,1] op_sel_hi:[1,0]
	v_pk_fma_f32 v[16:17], v[98:99], v[98:99], v[16:17] op_sel_hi:[1,1,0]
	v_pk_fma_f32 v[18:19], v[108:109], v[108:109], v[18:19] op_sel_hi:[1,1,0]
	v_pk_mul_f32 v[20:21], v[110:111], v[110:111]
	v_pk_mul_f32 v[22:23], v[124:125], v[124:125]
	v_mov_b32_e32 v13, v20
	v_mov_b32_e32 v15, v21
	v_mov_b32_e32 v17, v22
	v_mov_b32_e32 v19, v23
	v_pk_add_f32 v[12:13], v[12:13], v[14:15]
	v_pk_add_f32 v[14:15], v[16:17], v[18:19]
	v_sqrt_f32_e32 v25, v24
	v_pk_add_f32 v[12:13], v[12:13], v[14:15]
	v_and_b32_e32 v11, 0xffff0000, v45
	v_add_f32_e32 v12, v12, v13
	ds_bpermute_b32 v13, v193, v12
	v_pk_add_f32 v[8:9], v[8:9], v[10:11]
	s_waitcnt vmcnt(0)
; __device__ __forceinline__ void ph9_router(const Frame& F, const Args& A) {
;     ...
;         float rstd[4];
; #pragma unroll
;         for (int r = 0; r < 4; ++r) { float ss = 0.f;
; #pragma unroll
;             for (int j = 0; j < 8; ++j) ss += (hv[r][j].x * hv[r][j].x + hv[r][j].y * hv[r][j].y) + (hv[r][j].z * hv[r][j].z + hv[r][j].w * hv[r][j].w);
;             rstd[r] = 1.f / sqrtf(wave_sum(ss) * (1.f / DM) + EPS_); }
	v_lshlrev_b32_e32 v10, 16, v42
	v_and_b32_e32 v11, 0xffff0000, v42
	v_pk_add_f32 v[2:3], v[2:3], v[10:11]
	s_waitcnt lgkmcnt(0)
	v_add_f32_e32 v12, v12, v13
	ds_bpermute_b32 v13, v196, v12
	v_add_u32_e32 v11, -1, v25
	v_fma_f32 v14, -v11, v25, v24
	v_cmp_ge_f32_e64 s[0:1], 0, v14
	v_add_u32_e32 v14, 1, v25
	s_waitcnt lgkmcnt(0)
	v_add_f32_e32 v12, v12, v13
	ds_bpermute_b32 v13, v195, v12
	v_fma_f32 v15, -v14, v25, v24
	v_cndmask_b32_e64 v11, v25, v11, s[0:1]
	v_cmp_lt_f32_e64 s[0:1], 0, v15
	v_lshlrev_b32_e32 v10, 16, v43
	s_waitcnt lgkmcnt(0)
	v_add_f32_e32 v12, v12, v13
	ds_bpermute_b32 v13, v194, v12
	v_cndmask_b32_e64 v11, v11, v14, s[0:1]
	v_mul_f32_e32 v14, 0x37800000, v11
	v_cndmask_b32_e32 v11, v11, v14, vcc
	v_cmp_class_f32_e32 vcc, v24, v171
	s_waitcnt lgkmcnt(0)
	v_add_f32_e32 v12, v12, v13
	ds_bpermute_b32 v13, v197, v12
	v_cndmask_b32_e32 v22, v11, v24, vcc
	v_div_scale_f32 v23, s[0:1], v22, v22, 1.0
	v_rcp_f32_e32 v24, v23
	v_and_b32_e32 v11, 0xffff0000, v43
	v_pk_add_f32 v[4:5], v[4:5], v[10:11]
	v_mov_b32_e32 v14, v69
	v_fma_f32 v10, -v23, v24, 1.0
	v_fmac_f32_e32 v24, v10, v24
	s_waitcnt lgkmcnt(0)
	v_add_f32_e32 v10, v12, v13
	ds_bpermute_b32 v11, v198, v10
	v_mov_b32_e32 v12, v73
	v_mov_b32_e32 v13, v63
	v_pk_mul_f32 v[12:13], v[12:13], v[12:13]
	v_mov_b32_e32 v15, v65
	s_waitcnt lgkmcnt(0)
	v_add_f32_e32 v10, v10, v11
	v_fmamk_f32 v10, v10, 0x3a000000, v169
	v_mul_f32_e32 v11, 0x4f800000, v10
	v_cmp_gt_f32_e64 s[0:1], s47, v10
	v_pk_mul_f32 v[14:15], v[14:15], v[14:15]
	v_mul_f32_e32 v16, v59, v59
	v_cndmask_b32_e64 v30, v10, v11, s[0:1]
	v_mov_b32_e32 v10, v72
	v_mov_b32_e32 v11, v62
	v_pk_fma_f32 v[10:11], v[10:11], v[10:11], v[12:13]
	v_mov_b32_e32 v12, v68
	v_mov_b32_e32 v13, v64
	v_pk_fma_f32 v[12:13], v[12:13], v[12:13], v[14:15]
	v_mov_b32_e32 v14, v55
	v_mov_b32_e32 v15, v57
	v_pk_add_f32 v[10:11], v[10:11], v[12:13]
	v_mov_b32_e32 v12, v54
	v_mov_b32_e32 v13, v56
	v_pk_mul_f32 v[14:15], v[14:15], v[14:15]
	v_pk_add_f32 v[10:11], v[10:11], v[10:11] op_sel:[0,1] op_sel_hi:[1,0]
	v_pk_fma_f32 v[12:13], v[12:13], v[12:13], v[14:15]
	v_mul_f32_e32 v14, v51, v51
	v_pk_add_f32 v[12:13], v[12:13], v[12:13] op_sel:[0,1] op_sel_hi:[1,0]
	v_pk_fma_f32 v[14:15], v[50:51], v[50:51], v[14:15] op_sel_hi:[1,1,0]
	v_pk_fma_f32 v[16:17], v[58:59], v[58:59], v[16:17] op_sel_hi:[1,1,0]
	v_pk_mul_f32 v[18:19], v[66:67], v[66:67]
	v_pk_mul_f32 v[20:21], v[70:71], v[70:71]
	v_mov_b32_e32 v11, v18
	v_mov_b32_e32 v13, v19
	v_mov_b32_e32 v15, v20
	v_mov_b32_e32 v17, v21
	v_pk_add_f32 v[10:11], v[10:11], v[12:13]
	v_pk_add_f32 v[12:13], v[14:15], v[16:17]
	v_mov_b32_e32 v14, v113
	v_mov_b32_e32 v15, v127
	v_pk_add_f32 v[10:11], v[10:11], v[12:13]
	v_mov_b32_e32 v12, v112
	v_mov_b32_e32 v13, v126
	v_pk_mul_f32 v[14:15], v[14:15], v[14:15]
	v_mul_f32_e32 v16, v121, v121
	v_pk_fma_f32 v[12:13], v[12:13], v[12:13], v[14:15]
	v_mul_f32_e32 v14, v119, v119
	v_pk_add_f32 v[10:11], v[10:11], v[10:11] op_sel:[0,1] op_sel_hi:[1,0]
	v_pk_add_f32 v[12:13], v[12:13], v[12:13] op_sel:[0,1] op_sel_hi:[1,0]
	v_pk_fma_f32 v[14:15], v[118:119], v[118:119], v[14:15] op_sel_hi:[1,1,0]
	v_pk_fma_f32 v[16:17], v[120:121], v[120:121], v[16:17] op_sel_hi:[1,1,0]
	v_pk_mul_f32 v[18:19], v[136:137], v[136:137]
	v_pk_mul_f32 v[20:21], v[138:139], v[138:139]
	v_mov_b32_e32 v11, v18
	v_mov_b32_e32 v13, v19
	v_mov_b32_e32 v15, v20
	v_mov_b32_e32 v17, v21
	v_pk_add_f32 v[10:11], v[10:11], v[12:13]
	v_pk_add_f32 v[12:13], v[14:15], v[16:17]
	v_sqrt_f32_e32 v31, v30
	v_pk_add_f32 v[10:11], v[10:11], v[12:13]
	v_div_scale_f32 v25, vcc, 1.0, v22, 1.0
	v_add_f32_e32 v10, v10, v11
	ds_bpermute_b32 v11, v193, v10
	v_add_u32_e32 v13, -1, v31
	v_fma_f32 v14, -v13, v31, v30
	v_cmp_ge_f32_e64 s[4:5], 0, v14
	v_add_u32_e32 v14, 1, v31
	s_waitcnt lgkmcnt(0)
	v_add_f32_e32 v10, v10, v11
	ds_bpermute_b32 v11, v196, v10
	v_fma_f32 v15, -v14, v31, v30
	v_cndmask_b32_e64 v13, v31, v13, s[4:5]
	v_cmp_lt_f32_e64 s[4:5], 0, v15
	v_mul_f32_e32 v26, v25, v24
	s_waitcnt lgkmcnt(0)
	v_add_f32_e32 v10, v10, v11
	ds_bpermute_b32 v11, v195, v10
	v_cndmask_b32_e64 v13, v13, v14, s[4:5]
	v_fma_f32 v27, -v23, v26, v25
	v_mul_f32_e32 v14, 0x37800000, v13
	v_fmac_f32_e32 v26, v27, v24
	s_waitcnt lgkmcnt(0)
	v_add_f32_e32 v10, v10, v11
	ds_bpermute_b32 v11, v194, v10
	v_cndmask_b32_e64 v13, v13, v14, s[0:1]
	v_cmp_class_f32_e64 s[0:1], v30, v171
	v_fma_f32 v12, -v23, v26, v25
	v_div_fmas_f32 v12, v12, v24, v26
	s_waitcnt lgkmcnt(0)
	v_add_f32_e32 v10, v10, v11
	ds_bpermute_b32 v11, v197, v10
	v_cndmask_b32_e64 v25, v13, v30, s[0:1]
	v_div_scale_f32 v27, s[0:1], v25, v25, 1.0
	v_rcp_f32_e32 v30, v27
	s_waitcnt lgkmcnt(0)
	v_add_f32_e32 v10, v10, v11
	ds_bpermute_b32 v11, v198, v10
	v_div_fixup_f32 v130, v12, v22, 1.0
	v_fma_f32 v12, -v27, v30, 1.0
	v_fmac_f32_e32 v30, v12, v30
	v_mov_b32_e32 v12, v39
	s_waitcnt lgkmcnt(0)
; __device__ __forceinline__ void ph9_router(const Frame& F, const Args& A) {
;     ...
;         for (int r = 0; r < 4; ++r) { float ss = 0.f;
; #pragma unroll
;             for (int j = 0; j < 8; ++j) ss += (hv[r][j].x * hv[r][j].x + hv[r][j].y * hv[r][j].y) + (hv[r][j].z * hv[r][j].z + hv[r][j].w * hv[r][j].w);
;             rstd[r] = 1.f / sqrtf(wave_sum(ss) * (1.f / DM) + EPS_); }
; #pragma unroll
;         for (int j = 0; j < 8; ++j) { const int col = 4 * lane + 256 * j;
;             const f32x4 g = *(const f32x4*)(g2n + col), sh = *(const f32x4*)(MOD + 6144 + col), sc = *(const f32x4*)(MOD + 8192 + col);
;             const f32x4 gs1 = g * (sc + 1.f);
; #pragma unroll
;             for (int r = 0; r < 4; ++r) hv[r][j] = hv[r][j] * rstd[r] * gs1 + sh;
;             __builtin_amdgcn_sched_barrier(0); }
	v_add_f32_e32 v10, v10, v11
	v_fmamk_f32 v10, v10, 0x3a000000, v169
	v_mul_f32_e32 v11, 0x4f800000, v10
	v_cmp_gt_f32_e64 s[4:5], s47, v10
	v_mov_b32_e32 v13, v33
	v_pk_mul_f32 v[12:13], v[12:13], v[12:13]
	v_cndmask_b32_e64 v48, v10, v11, s[4:5]
	v_mov_b32_e32 v10, v38
	v_mov_b32_e32 v11, v32
	v_mov_b32_e32 v14, v41
	v_mov_b32_e32 v15, v29
	v_pk_fma_f32 v[10:11], v[10:11], v[10:11], v[12:13]
	v_mov_b32_e32 v12, v40
	v_mov_b32_e32 v13, v28
	v_pk_mul_f32 v[14:15], v[14:15], v[14:15]
	v_mul_f32_e32 v16, v61, v61
	v_pk_fma_f32 v[12:13], v[12:13], v[12:13], v[14:15]
	v_mov_b32_e32 v14, v35
	v_mov_b32_e32 v15, v37
	v_pk_add_f32 v[10:11], v[10:11], v[12:13]
	v_mov_b32_e32 v12, v34
	v_mov_b32_e32 v13, v36
	v_pk_mul_f32 v[14:15], v[14:15], v[14:15]
	v_pk_add_f32 v[10:11], v[10:11], v[10:11] op_sel:[0,1] op_sel_hi:[1,0]
	v_pk_fma_f32 v[12:13], v[12:13], v[12:13], v[14:15]
	v_mul_f32_e32 v14, v47, v47
	v_pk_add_f32 v[12:13], v[12:13], v[12:13] op_sel:[0,1] op_sel_hi:[1,0]
	v_pk_fma_f32 v[14:15], v[46:47], v[46:47], v[14:15] op_sel_hi:[1,1,0]
	v_pk_fma_f32 v[16:17], v[60:61], v[60:61], v[16:17] op_sel_hi:[1,1,0]
	v_pk_mul_f32 v[18:19], v[74:75], v[74:75]
	v_pk_mul_f32 v[20:21], v[164:165], v[164:165]
	v_mov_b32_e32 v11, v18
	v_mov_b32_e32 v13, v19
	v_mov_b32_e32 v15, v20
	v_mov_b32_e32 v17, v21
	v_pk_add_f32 v[10:11], v[10:11], v[12:13]
	v_pk_add_f32 v[12:13], v[14:15], v[16:17]
	v_mov_b32_e32 v14, v153
	v_mov_b32_e32 v15, v167
	v_pk_add_f32 v[10:11], v[10:11], v[12:13]
	v_mov_b32_e32 v12, v152
	v_mov_b32_e32 v13, v166
	v_pk_mul_f32 v[14:15], v[14:15], v[14:15]
	v_pk_add_f32 v[10:11], v[10:11], v[10:11] op_sel:[0,1] op_sel_hi:[1,0]
	v_pk_fma_f32 v[12:13], v[12:13], v[12:13], v[14:15]
	v_mul_f32_e32 v14, v7, v7
	v_pk_fma_f32 v[18:19], v[6:7], v[6:7], v[14:15] op_sel_hi:[1,1,0]
	v_mul_f32_e32 v14, v9, v9
	v_pk_add_f32 v[12:13], v[12:13], v[12:13] op_sel:[0,1] op_sel_hi:[1,0]
	v_pk_fma_f32 v[20:21], v[8:9], v[8:9], v[14:15] op_sel_hi:[1,1,0]
	v_pk_mul_f32 v[14:15], v[2:3], v[2:3]
	v_pk_mul_f32 v[16:17], v[4:5], v[4:5]
	v_mov_b32_e32 v11, v14
	v_mov_b32_e32 v13, v15
	v_pk_add_f32 v[22:23], v[10:11], v[12:13]
	v_lshlrev_b32_e32 v10, 2, v132
	v_ashrrev_i32_e32 v11, 31, v10
	v_lshlrev_b64 v[14:15], 2, v[10:11]
	v_lshl_add_u64 v[174:175], s[34:35], 0, v[14:15]
	v_lshl_add_u64 v[176:177], s[36:37], 0, v[14:15]
	global_load_dwordx4 v[42:45], v[174:175], off
	global_load_dwordx4 v[10:13], v[176:177], off
	v_lshl_add_u64 v[178:179], s[70:71], 0, v[14:15]
	v_mov_b32_e32 v19, v16
	v_mov_b32_e32 v21, v17
	global_load_dwordx4 v[14:17], v[178:179], off
	s_movk_i32 s98, 0x1000
	s_mov_b32 s99, 0
	global_load_dwordx4 v[200:203], v[176:177], off offset:1024
	global_load_dwordx4 v[204:207], v[178:179], off offset:1024
	global_load_dwordx4 v[208:211], v[174:175], off offset:1024
	global_load_dwordx4 v[212:215], v[176:177], off offset:2048
	global_load_dwordx4 v[216:219], v[178:179], off offset:2048
	global_load_dwordx4 v[220:223], v[174:175], off offset:2048
	global_load_dwordx4 v[224:227], v[176:177], off offset:3072
	global_load_dwordx4 v[228:231], v[178:179], off offset:3072
	global_load_dwordx4 v[232:235], v[174:175], off offset:3072
	v_lshl_add_u64 v[248:249], v[178:179], 0, s[98:99]
	v_lshl_add_u64 v[250:251], v[176:177], 0, s[98:99]
	v_lshl_add_u64 v[252:253], v[174:175], 0, s[98:99]
	global_load_dwordx4 v[236:239], v[248:249], off
	global_load_dwordx4 v[240:243], v[250:251], off
	global_load_dwordx4 v[244:247], v[252:253], off
	v_pk_add_f32 v[18:19], v[18:19], v[20:21]
	v_sqrt_f32_e32 v49, v48
	v_pk_add_f32 v[18:19], v[22:23], v[18:19]
	v_div_scale_f32 v24, vcc, 1.0, v25, 1.0
	v_add_f32_e32 v18, v18, v19
	ds_bpermute_b32 v19, v193, v18
	v_add_u32_e32 v21, -1, v49
	v_fma_f32 v22, -v21, v49, v48
	v_cmp_ge_f32_e64 s[0:1], 0, v22
	v_add_u32_e32 v22, 1, v49
	s_waitcnt lgkmcnt(0)
	v_add_f32_e32 v18, v18, v19
	ds_bpermute_b32 v19, v196, v18
	v_fma_f32 v23, -v22, v49, v48
	v_cndmask_b32_e64 v21, v49, v21, s[0:1]
	v_cmp_lt_f32_e64 s[0:1], 0, v23
	v_mul_f32_e32 v26, v24, v30
	s_waitcnt lgkmcnt(0)
	v_add_f32_e32 v18, v18, v19
	ds_bpermute_b32 v19, v195, v18
	v_cndmask_b32_e64 v21, v21, v22, s[0:1]
	v_mul_f32_e32 v22, 0x37800000, v21
	v_cndmask_b32_e64 v21, v21, v22, s[4:5]
	v_cmp_class_f32_e64 s[0:1], v48, v171
	s_waitcnt lgkmcnt(0)
	v_add_f32_e32 v18, v18, v19
	ds_bpermute_b32 v19, v194, v18
	v_cndmask_b32_e64 v21, v21, v48, s[0:1]
	v_div_scale_f32 v22, s[0:1], v21, v21, 1.0
	v_fma_f32 v31, -v27, v26, v24
	s_waitcnt lgkmcnt(0)
	v_add_f32_e32 v18, v18, v19
	ds_bpermute_b32 v19, v197, v18
	v_rcp_f32_e32 v23, v22
	v_fmac_f32_e32 v26, v31, v30
	v_fma_f32 v20, -v27, v26, v24
	v_div_fmas_f32 v20, v20, v30, v26
	s_waitcnt lgkmcnt(0)
	v_add_f32_e32 v18, v18, v19
	ds_bpermute_b32 v19, v198, v18
	v_div_fixup_f32 v168, v20, v25, 1.0
	v_fma_f32 v20, -v22, v23, 1.0
	v_fmac_f32_e32 v23, v20, v23
	v_div_scale_f32 v20, vcc, 1.0, v21, 1.0
	s_waitcnt lgkmcnt(0)
	v_add_f32_e32 v18, v18, v19
	v_fmamk_f32 v18, v18, 0x3a000000, v169
	v_mul_f32_e32 v19, 0x4f800000, v18
	v_cmp_gt_f32_e64 s[0:1], s47, v18
	v_mul_f32_e32 v24, v20, v23
	v_fma_f32 v25, -v22, v24, v20
	v_cndmask_b32_e64 v18, v18, v19, s[0:1]
	v_sqrt_f32_e32 v19, v18
	v_fmac_f32_e32 v24, v25, v23
	v_fma_f32 v20, -v22, v24, v20
	v_div_fmas_f32 v20, v20, v23, v24
	v_add_u32_e32 v22, -1, v19
	v_fma_f32 v25, -v22, v19, v18
	v_cmp_ge_f32_e64 s[4:5], 0, v25
	v_add_u32_e32 v25, 1, v19
	v_div_fixup_f32 v170, v20, v21, 1.0
	v_cndmask_b32_e64 v22, v19, v22, s[4:5]
	v_fma_f32 v19, -v25, v19, v18
	v_cmp_lt_f32_e64 s[4:5], 0, v19
	s_waitcnt vmcnt(13)
; __device__ __forceinline__ void ph9_router(const Frame& F, const Args& A) {
;     ...
;         for (int j = 0; j < 8; ++j) { const int col = 4 * lane + 256 * j;
;             const f32x4 g = *(const f32x4*)(g2n + col), sh = *(const f32x4*)(MOD + 6144 + col), sc = *(const f32x4*)(MOD + 8192 + col);
;             const f32x4 gs1 = g * (sc + 1.f);
; #pragma unroll
;             for (int r = 0; r < 4; ++r) hv[r][j] = hv[r][j] * rstd[r] * gs1 + sh;
;             __builtin_amdgcn_sched_barrier(0); }
	v_pk_add_f32 v[10:11], v[10:11], 1.0 op_sel_hi:[1,0]
	v_cndmask_b32_e64 v19, v22, v25, s[4:5]
	v_mul_f32_e32 v22, 0x37800000, v19
	v_cndmask_b32_e64 v19, v19, v22, s[0:1]
	v_cmp_class_f32_e64 s[0:1], v18, v171
	v_pk_add_f32 v[12:13], v[12:13], 1.0 op_sel_hi:[1,0]
	s_nop 0
	v_cndmask_b32_e64 v18, v19, v18, s[0:1]
	v_div_scale_f32 v19, s[0:1], v18, v18, 1.0
	v_rcp_f32_e32 v22, v19
	s_waitcnt vmcnt(12)
	v_pk_mul_f32 v[12:13], v[16:17], v[12:13]
	v_fma_f32 v20, -v19, v22, 1.0
	v_fmac_f32_e32 v22, v20, v22
	v_div_scale_f32 v20, vcc, 1.0, v18, 1.0
	v_mul_f32_e32 v21, v20, v22
	v_fma_f32 v23, -v19, v21, v20
	v_fmac_f32_e32 v21, v23, v22
	v_fma_f32 v19, -v19, v21, v20
	v_div_fmas_f32 v19, v19, v22, v21
	v_div_fixup_f32 v172, v19, v18, 1.0
	v_pk_mul_f32 v[18:19], v[14:15], v[10:11]
	v_pk_mul_f32 v[10:11], v[156:157], v[130:131] op_sel_hi:[1,0]
	v_pk_mul_f32 v[14:15], v[158:159], v[130:131] op_sel_hi:[1,0]
	v_pk_fma_f32 v[30:31], v[10:11], v[18:19], v[42:43]
	v_pk_mul_f32 v[10:11], v[160:161], v[168:169] op_sel_hi:[1,0]
	v_pk_fma_f32 v[26:27], v[14:15], v[12:13], v[44:45]
	v_pk_mul_f32 v[14:15], v[162:163], v[168:169] op_sel_hi:[1,0]
	v_pk_fma_f32 v[24:25], v[10:11], v[18:19], v[42:43]
	v_pk_mul_f32 v[10:11], v[72:73], v[170:171] op_sel_hi:[1,0]
	v_pk_fma_f32 v[20:21], v[14:15], v[12:13], v[44:45]
	v_pk_mul_f32 v[14:15], v[68:69], v[170:171] op_sel_hi:[1,0]
	v_pk_fma_f32 v[16:17], v[10:11], v[18:19], v[42:43]
	v_pk_mul_f32 v[22:23], v[38:39], v[172:173] op_sel_hi:[1,0]
	v_pk_mul_f32 v[10:11], v[40:41], v[172:173] op_sel_hi:[1,0]
	v_pk_fma_f32 v[14:15], v[14:15], v[12:13], v[44:45]
	v_pk_fma_f32 v[10:11], v[12:13], v[10:11], v[44:45]
	v_pk_fma_f32 v[12:13], v[18:19], v[22:23], v[42:43]
	s_waitcnt vmcnt(9)
	v_mov_b64_e32 v[38:39], v[200:201]
	v_mov_b64_e32 v[40:41], v[202:203]
	v_mov_b64_e32 v[42:43], v[204:205]
	v_mov_b64_e32 v[44:45], v[206:207]
	v_mov_b64_e32 v[156:157], v[208:209]
	v_mov_b64_e32 v[158:159], v[210:211]
	global_load_dwordx4 v[200:203], v[250:251], off offset:1024
	global_load_dwordx4 v[204:207], v[248:249], off offset:1024
	global_load_dwordx4 v[208:211], v[252:253], off offset:1024
	v_pk_mul_f32 v[76:77], v[32:33], v[172:173] op_sel_hi:[1,0]
	v_pk_mul_f32 v[80:81], v[28:29], v[172:173] op_sel_hi:[1,0]
	v_pk_mul_f32 v[18:19], v[146:147], v[130:131] op_sel_hi:[1,0]
	v_pk_mul_f32 v[22:23], v[148:149], v[130:131] op_sel_hi:[1,0]
	v_pk_mul_f32 v[68:69], v[150:151], v[168:169] op_sel_hi:[1,0]
	v_pk_mul_f32 v[72:73], v[154:155], v[168:169] op_sel_hi:[1,0]
	v_pk_mul_f32 v[62:63], v[62:63], v[170:171] op_sel_hi:[1,0]
	v_pk_mul_f32 v[64:65], v[64:65], v[170:171] op_sel_hi:[1,0]
	v_pk_add_f32 v[28:29], v[40:41], 1.0 op_sel_hi:[1,0]
	v_pk_add_f32 v[32:33], v[38:39], 1.0 op_sel_hi:[1,0]
	v_pk_mul_f32 v[44:45], v[44:45], v[28:29]
	v_pk_mul_f32 v[42:43], v[42:43], v[32:33]
	v_pk_fma_f32 v[48:49], v[22:23], v[44:45], v[158:159]
	v_pk_fma_f32 v[52:53], v[18:19], v[42:43], v[156:157]
	v_pk_fma_f32 v[38:39], v[72:73], v[44:45], v[158:159]
	v_pk_fma_f32 v[40:41], v[68:69], v[42:43], v[156:157]
	v_pk_fma_f32 v[28:29], v[64:65], v[44:45], v[158:159]
	v_pk_fma_f32 v[32:33], v[62:63], v[42:43], v[156:157]
	v_pk_fma_f32 v[18:19], v[80:81], v[44:45], v[158:159]
	v_pk_fma_f32 v[22:23], v[76:77], v[42:43], v[156:157]
	s_waitcnt vmcnt(9)
	v_mov_b64_e32 v[42:43], v[212:213]
	v_mov_b64_e32 v[44:45], v[214:215]
	v_mov_b64_e32 v[62:63], v[216:217]
	v_mov_b64_e32 v[64:65], v[218:219]
	v_mov_b64_e32 v[146:147], v[220:221]
	v_mov_b64_e32 v[148:149], v[222:223]
	global_load_dwordx4 v[212:215], v[250:251], off offset:2048
	global_load_dwordx4 v[216:219], v[248:249], off offset:2048
	global_load_dwordx4 v[220:223], v[252:253], off offset:2048
	v_pk_mul_f32 v[72:73], v[142:143], v[130:131] op_sel_hi:[1,0]
	v_pk_mul_f32 v[142:143], v[34:35], v[172:173] op_sel_hi:[1,0]
	v_pk_mul_f32 v[34:35], v[36:37], v[172:173] op_sel_hi:[1,0]
	v_pk_mul_f32 v[68:69], v[140:141], v[130:131] op_sel_hi:[1,0]
	v_pk_mul_f32 v[76:77], v[128:129], v[168:169] op_sel_hi:[1,0]
	v_pk_mul_f32 v[80:81], v[144:145], v[168:169] op_sel_hi:[1,0]
	v_pk_mul_f32 v[128:129], v[54:55], v[170:171] op_sel_hi:[1,0]
	v_pk_mul_f32 v[140:141], v[56:57], v[170:171] op_sel_hi:[1,0]
	v_pk_add_f32 v[36:37], v[44:45], 1.0 op_sel_hi:[1,0]
	v_pk_add_f32 v[42:43], v[42:43], 1.0 op_sel_hi:[1,0]
	v_pk_mul_f32 v[36:37], v[64:65], v[36:37]
	v_pk_mul_f32 v[144:145], v[62:63], v[42:43]
	v_pk_fma_f32 v[62:63], v[72:73], v[36:37], v[148:149]
	v_pk_fma_f32 v[64:65], v[68:69], v[144:145], v[146:147]
	v_pk_fma_f32 v[54:55], v[80:81], v[36:37], v[148:149]
	v_pk_fma_f32 v[56:57], v[76:77], v[144:145], v[146:147]
	v_pk_fma_f32 v[42:43], v[140:141], v[36:37], v[148:149]
	v_pk_fma_f32 v[44:45], v[128:129], v[144:145], v[146:147]
	v_pk_fma_f32 v[34:35], v[34:35], v[36:37], v[148:149]
	v_pk_fma_f32 v[36:37], v[142:143], v[144:145], v[146:147]
	s_waitcnt vmcnt(9)
; __device__ __forceinline__ void ph9_router(const Frame& F, const Args& A) {
;     ...
;         for (int j = 0; j < 8; ++j) { const int col = 4 * lane + 256 * j;
;             const f32x4 g = *(const f32x4*)(g2n + col), sh = *(const f32x4*)(MOD + 6144 + col), sc = *(const f32x4*)(MOD + 8192 + col);
;             const f32x4 gs1 = g * (sc + 1.f);
; #pragma unroll
;             for (int r = 0; r < 4; ++r) hv[r][j] = hv[r][j] * rstd[r] * gs1 + sh;
;             __builtin_amdgcn_sched_barrier(0); }
	v_mov_b64_e32 v[140:141], v[224:225]
	v_mov_b64_e32 v[142:143], v[226:227]
	v_mov_b64_e32 v[144:145], v[228:229]
	v_mov_b64_e32 v[146:147], v[230:231]
	v_mov_b64_e32 v[148:149], v[232:233]
	v_mov_b64_e32 v[150:151], v[234:235]
	global_load_dwordx4 v[224:227], v[250:251], off offset:3072
	global_load_dwordx4 v[228:231], v[248:249], off offset:3072
	global_load_dwordx4 v[232:235], v[252:253], off offset:3072
	v_pk_mul_f32 v[68:69], v[104:105], v[130:131] op_sel_hi:[1,0]
	v_pk_mul_f32 v[104:105], v[46:47], v[172:173] op_sel_hi:[1,0]
	v_pk_mul_f32 v[46:47], v[60:61], v[172:173] op_sel_hi:[1,0]
	v_pk_mul_f32 v[72:73], v[116:117], v[130:131] op_sel_hi:[1,0]
	v_pk_mul_f32 v[86:87], v[86:87], v[168:169] op_sel_hi:[1,0]
	v_pk_mul_f32 v[88:89], v[88:89], v[168:169] op_sel_hi:[1,0]
	v_pk_mul_f32 v[50:51], v[50:51], v[170:171] op_sel_hi:[1,0]
	v_pk_mul_f32 v[58:59], v[58:59], v[170:171] op_sel_hi:[1,0]
	v_pk_add_f32 v[60:61], v[142:143], 1.0 op_sel_hi:[1,0]
	v_pk_add_f32 v[76:77], v[140:141], 1.0 op_sel_hi:[1,0]
	v_pk_mul_f32 v[116:117], v[146:147], v[60:61]
	v_pk_mul_f32 v[128:129], v[144:145], v[76:77]
	v_pk_fma_f32 v[76:77], v[72:73], v[116:117], v[150:151]
	v_pk_fma_f32 v[80:81], v[68:69], v[128:129], v[148:149]
	v_pk_fma_f32 v[68:69], v[88:89], v[116:117], v[150:151]
	v_pk_fma_f32 v[72:73], v[86:87], v[128:129], v[148:149]
	v_pk_fma_f32 v[58:59], v[58:59], v[116:117], v[150:151]
	v_pk_fma_f32 v[60:61], v[50:51], v[128:129], v[148:149]
	v_pk_fma_f32 v[46:47], v[46:47], v[116:117], v[150:151]
	v_pk_fma_f32 v[50:51], v[104:105], v[128:129], v[148:149]
	v_add_co_u32_e32 v148, vcc, s46, v178
	v_pk_mul_f32 v[104:105], v[96:97], v[130:131] op_sel_hi:[1,0]
	s_nop 0
	v_addc_co_u32_e32 v149, vcc, 0, v179, vcc
	v_add_co_u32_e32 v150, vcc, s46, v176
	s_waitcnt vmcnt(9)
	v_mov_b64_e32 v[86:87], v[236:237]
	v_mov_b64_e32 v[88:89], v[238:239]
	s_nop 0
	v_addc_co_u32_e32 v151, vcc, 0, v177, vcc
	v_mov_b64_e32 v[140:141], v[240:241]
	v_mov_b64_e32 v[142:143], v[242:243]
	v_add_co_u32_e32 v154, vcc, s46, v174
	v_pk_mul_f32 v[96:97], v[102:103], v[130:131] op_sel_hi:[1,0]
	s_nop 0
	v_addc_co_u32_e32 v155, vcc, 0, v175, vcc
	v_mov_b64_e32 v[144:145], v[244:245]
	v_mov_b64_e32 v[146:147], v[246:247]
	v_pk_mul_f32 v[102:103], v[100:101], v[168:169] op_sel_hi:[1,0]
	v_pk_mul_f32 v[116:117], v[74:75], v[172:173] op_sel_hi:[1,0]
	v_pk_mul_f32 v[78:79], v[78:79], v[168:169] op_sel_hi:[1,0]
	v_pk_mul_f32 v[66:67], v[66:67], v[170:171] op_sel_hi:[1,0]
	v_pk_mul_f32 v[70:71], v[70:71], v[170:171] op_sel_hi:[1,0]
	v_pk_mul_f32 v[128:129], v[164:165], v[172:173] op_sel_hi:[1,0]
	v_pk_add_f32 v[74:75], v[142:143], 1.0 op_sel_hi:[1,0]
	v_pk_add_f32 v[100:101], v[140:141], 1.0 op_sel_hi:[1,0]
	v_pk_mul_f32 v[140:141], v[88:89], v[74:75]
	v_pk_mul_f32 v[142:143], v[86:87], v[100:101]
	v_pk_fma_f32 v[96:97], v[96:97], v[140:141], v[146:147]
	v_pk_fma_f32 v[100:101], v[104:105], v[142:143], v[144:145]
	v_pk_fma_f32 v[86:87], v[102:103], v[140:141], v[146:147]
	v_pk_fma_f32 v[88:89], v[78:79], v[142:143], v[144:145]
	v_pk_fma_f32 v[74:75], v[70:71], v[140:141], v[146:147]
	v_pk_fma_f32 v[78:79], v[66:67], v[142:143], v[144:145]
	v_pk_fma_f32 v[66:67], v[128:129], v[140:141], v[146:147]
	v_pk_fma_f32 v[70:71], v[116:117], v[142:143], v[144:145]
	s_waitcnt vmcnt(6)
	v_mov_b64_e32 v[102:103], v[200:201]
	v_mov_b64_e32 v[104:105], v[202:203]
	v_mov_b64_e32 v[140:141], v[204:205]
	v_mov_b64_e32 v[142:143], v[206:207]
	v_mov_b64_e32 v[144:145], v[208:209]
	v_mov_b64_e32 v[146:147], v[210:211]
	v_pk_mul_f32 v[90:91], v[90:91], v[130:131] op_sel_hi:[1,0]
	v_pk_mul_f32 v[92:93], v[92:93], v[130:131] op_sel_hi:[1,0]
	v_pk_mul_f32 v[82:83], v[82:83], v[168:169] op_sel_hi:[1,0]
	v_pk_mul_f32 v[84:85], v[84:85], v[168:169] op_sel_hi:[1,0]
	v_pk_mul_f32 v[128:129], v[112:113], v[170:171] op_sel_hi:[1,0]
	v_pk_mul_f32 v[126:127], v[126:127], v[170:171] op_sel_hi:[1,0]
	v_pk_mul_f32 v[152:153], v[152:153], v[172:173] op_sel_hi:[1,0]
	v_pk_mul_f32 v[156:157], v[166:167], v[172:173] op_sel_hi:[1,0]
	v_pk_add_f32 v[104:105], v[104:105], 1.0 op_sel_hi:[1,0]
	v_pk_add_f32 v[102:103], v[102:103], 1.0 op_sel_hi:[1,0]
	v_pk_mul_f32 v[142:143], v[142:143], v[104:105]
	v_pk_mul_f32 v[140:141], v[140:141], v[102:103]
	v_pk_fma_f32 v[112:113], v[92:93], v[142:143], v[146:147]
	v_pk_fma_f32 v[116:117], v[90:91], v[140:141], v[144:145]
	v_pk_fma_f32 v[102:103], v[84:85], v[142:143], v[146:147]
	v_pk_fma_f32 v[104:105], v[82:83], v[140:141], v[144:145]
	v_pk_fma_f32 v[90:91], v[126:127], v[142:143], v[146:147]
	v_pk_fma_f32 v[92:93], v[128:129], v[140:141], v[144:145]
	v_pk_fma_f32 v[82:83], v[156:157], v[142:143], v[146:147]
	v_pk_fma_f32 v[84:85], v[152:153], v[140:141], v[144:145]
	s_waitcnt vmcnt(3)
; __device__ __forceinline__ void ph9_router(const Frame& F, const Args& A) {
;     ...
;         for (int j = 0; j < 8; ++j) { const int col = 4 * lane + 256 * j;
;             const f32x4 g = *(const f32x4*)(g2n + col), sh = *(const f32x4*)(MOD + 6144 + col), sc = *(const f32x4*)(MOD + 8192 + col);
;             const f32x4 gs1 = g * (sc + 1.f);
; #pragma unroll
;             for (int r = 0; r < 4; ++r) hv[r][j] = hv[r][j] * rstd[r] * gs1 + sh;
;             __builtin_amdgcn_sched_barrier(0); }
;         float lgv[2];
; #pragma unroll 1
;         for (int half = 0; half < 2; ++half) {
;             if (half == 1) { __syncthreads();
;               const f32x4* src = (const f32x4*)(WRT + (size_t)16 * DM);
; #pragma unroll 1
;               for (int i0 = 0; i0 < 16; i0 += 8) { f32x4 t8[8];
; #pragma unroll
;                 for (int i = 0; i < 8; ++i) t8[i] = src[tid + 512 * (i0 + i)];
; #pragma unroll
;                 for (int i = 0; i < 8; ++i) wl[tid + 512 * (i0 + i)] = t8[i]; } }
;             __syncthreads();
;             float mine = 0.f;
;             const bool b0 = lane & 1, b1 = lane & 2, b4 = lane & 16, b5 = lane & 32;
	v_mov_b64_e32 v[126:127], v[212:213]
	v_mov_b64_e32 v[128:129], v[214:215]
	v_mov_b64_e32 v[140:141], v[216:217]
	v_mov_b64_e32 v[142:143], v[218:219]
	v_mov_b64_e32 v[144:145], v[220:221]
	v_mov_b64_e32 v[146:147], v[222:223]
	v_pk_mul_f32 v[152:153], v[118:119], v[170:171] op_sel_hi:[1,0]
	v_pk_mul_f32 v[156:157], v[120:121], v[170:171] op_sel_hi:[1,0]
	v_pk_mul_f32 v[94:95], v[94:95], v[130:131] op_sel_hi:[1,0]
	v_pk_mul_f32 v[106:107], v[106:107], v[130:131] op_sel_hi:[1,0]
	v_pk_mul_f32 v[98:99], v[98:99], v[168:169] op_sel_hi:[1,0]
	v_pk_mul_f32 v[108:109], v[108:109], v[168:169] op_sel_hi:[1,0]
	v_pk_mul_f32 v[6:7], v[6:7], v[172:173] op_sel_hi:[1,0]
	v_pk_mul_f32 v[8:9], v[8:9], v[172:173] op_sel_hi:[1,0]
	v_pk_add_f32 v[118:119], v[128:129], 1.0 op_sel_hi:[1,0]
	v_pk_add_f32 v[120:121], v[126:127], 1.0 op_sel_hi:[1,0]
	v_pk_mul_f32 v[142:143], v[142:143], v[118:119]
	v_pk_mul_f32 v[140:141], v[140:141], v[120:121]
	v_pk_fma_f32 v[126:127], v[106:107], v[142:143], v[146:147]
	v_pk_fma_f32 v[128:129], v[94:95], v[140:141], v[144:145]
	v_pk_fma_f32 v[118:119], v[108:109], v[142:143], v[146:147]
	v_pk_fma_f32 v[120:121], v[98:99], v[140:141], v[144:145]
	v_pk_fma_f32 v[106:107], v[156:157], v[142:143], v[146:147]
	v_pk_fma_f32 v[108:109], v[152:153], v[140:141], v[144:145]
	v_pk_fma_f32 v[94:95], v[8:9], v[142:143], v[146:147]
	v_pk_fma_f32 v[98:99], v[6:7], v[140:141], v[144:145]
	s_waitcnt vmcnt(0)
	v_mov_b64_e32 v[6:7], v[224:225]
	v_mov_b64_e32 v[8:9], v[226:227]
	v_mov_b64_e32 v[140:141], v[228:229]
	v_mov_b64_e32 v[142:143], v[230:231]
	v_mov_b64_e32 v[144:145], v[232:233]
	v_mov_b64_e32 v[146:147], v[234:235]
	v_pk_mul_f32 v[114:115], v[114:115], v[130:131] op_sel_hi:[1,0]
	v_pk_mul_f32 v[122:123], v[122:123], v[130:131] op_sel_hi:[1,0]
	v_pk_mul_f32 v[110:111], v[110:111], v[168:169] op_sel_hi:[1,0]
	v_pk_mul_f32 v[124:125], v[124:125], v[168:169] op_sel_hi:[1,0]
	v_pk_mul_f32 v[148:149], v[136:137], v[170:171] op_sel_hi:[1,0]
	v_pk_mul_f32 v[150:151], v[138:139], v[170:171] op_sel_hi:[1,0]
	v_pk_mul_f32 v[2:3], v[2:3], v[172:173] op_sel_hi:[1,0]
	v_pk_mul_f32 v[4:5], v[4:5], v[172:173] op_sel_hi:[1,0]
	v_pk_add_f32 v[8:9], v[8:9], 1.0 op_sel_hi:[1,0]
	v_pk_add_f32 v[6:7], v[6:7], 1.0 op_sel_hi:[1,0]
	v_pk_mul_f32 v[8:9], v[142:143], v[8:9]
	v_pk_mul_f32 v[6:7], v[140:141], v[6:7]
	v_pk_fma_f32 v[140:141], v[122:123], v[8:9], v[146:147]
	v_pk_fma_f32 v[142:143], v[114:115], v[6:7], v[144:145]
	v_pk_fma_f32 v[136:137], v[124:125], v[8:9], v[146:147]
	v_pk_fma_f32 v[138:139], v[110:111], v[6:7], v[144:145]
	v_pk_fma_f32 v[122:123], v[150:151], v[8:9], v[146:147]
	v_pk_fma_f32 v[124:125], v[148:149], v[6:7], v[144:145]
	v_pk_fma_f32 v[110:111], v[4:5], v[8:9], v[146:147]
	v_pk_fma_f32 v[114:115], v[2:3], v[6:7], v[144:145]
	v_and_b32_e32 v2, 1, v132
	v_cmp_eq_u32_e64 s[4:5], 0, v2
	v_and_b32_e32 v2, 2, v132
	v_cmp_eq_u32_e64 s[6:7], 0, v2
	v_and_b32_e32 v2, 16, v132
	v_cmp_eq_u32_e64 s[8:9], 0, v2
	v_and_b32_e32 v2, 32, v132
	v_cmp_eq_u32_e64 s[10:11], 0, v2
	v_lshlrev_b32_e32 v2, 13, v132
	v_lshl_add_u32 v157, v132, 4, 0
	v_and_b32_e32 v156, 15, v132
	v_and_b32_e32 v158, 0x18000, v2
	s_mov_b64 s[0:1], -1
	s_mov_b64 s[12:13], 0
	s_mov_b32 s98, s38
	s_mov_b32 s99, s39
	global_load_dwordx4 v[200:203], v135, s[98:99]
	s_add_u32 s98, s98, 0x2000
	s_addc_u32 s99, s99, 0
	global_load_dwordx4 v[204:207], v135, s[98:99]
	s_add_u32 s98, s98, 0x2000
	s_addc_u32 s99, s99, 0
	global_load_dwordx4 v[208:211], v135, s[98:99]
	s_add_u32 s98, s98, 0x2000
	s_addc_u32 s99, s99, 0
	global_load_dwordx4 v[212:215], v135, s[98:99]
	s_add_u32 s98, s98, 0x2000
	s_addc_u32 s99, s99, 0
	global_load_dwordx4 v[216:219], v135, s[98:99]
	s_add_u32 s98, s98, 0x2000
	s_addc_u32 s99, s99, 0
	global_load_dwordx4 v[220:223], v135, s[98:99]
	s_add_u32 s98, s98, 0x2000
	s_addc_u32 s99, s99, 0
	global_load_dwordx4 v[224:227], v135, s[98:99]
	s_add_u32 s98, s98, 0x2000
	s_addc_u32 s99, s99, 0
	global_load_dwordx4 v[246:249], v135, s[98:99]
	s_add_u32 s98, s98, 0x2000
	s_addc_u32 s99, s99, 0
	global_load_dwordx4 v[250:253], v135, s[98:99]
	s_cbranch_execnz .LBB0_1198
.LBB0_1196:
	s_add_u32 s98, s38, 0x12000
	s_addc_u32 s99, s39, 0
	global_load_dwordx4 v[2:5], v135, s[98:99]
	s_add_u32 s98, s98, 0x2000
	s_addc_u32 s99, s99, 0
	global_load_dwordx4 v[6:9], v135, s[98:99]
	s_add_u32 s98, s98, 0x2000
	s_addc_u32 s99, s99, 0
	global_load_dwordx4 v[144:147], v135, s[98:99]
	s_add_u32 s98, s98, 0x2000
	s_addc_u32 s99, s99, 0
	global_load_dwordx4 v[148:151], v135, s[98:99]
	s_add_u32 s98, s98, 0x2000
	s_addc_u32 s99, s99, 0
	global_load_dwordx4 v[152:155], v135, s[98:99]
	s_add_u32 s98, s98, 0x2000
	s_addc_u32 s99, s99, 0
	global_load_dwordx4 v[160:163], v135, s[98:99]
	s_add_u32 s98, s98, 0x2000
	s_addc_u32 s99, s99, 0
	global_load_dwordx4 v[164:167], v135, s[98:99]
	v_add_u32_e32 v130, 0x10000, v135
	s_mov_b32 s33, 8
	s_mov_b64 s[14:15], 0
	s_barrier
	s_waitcnt vmcnt(7)
	ds_write_b128 v135, v[200:203]
	ds_write_b128 v135, v[204:207] offset:8192
	ds_write_b128 v135, v[208:211] offset:16384
	ds_write_b128 v135, v[212:215] offset:24576
	ds_write_b128 v135, v[216:219] offset:32768
	ds_write_b128 v135, v[220:223] offset:40960
	ds_write_b128 v135, v[224:227] offset:49152
	ds_write_b128 v135, v[246:249] offset:57344
	ds_write_b128 v130, v[250:253]
	s_waitcnt vmcnt(0)
	ds_write_b128 v130, v[2:5] offset:8192
	ds_write_b128 v130, v[6:9] offset:16384
	ds_write_b128 v130, v[144:147] offset:24576
	ds_write_b128 v130, v[148:151] offset:32768
	ds_write_b128 v130, v[152:155] offset:40960
	ds_write_b128 v130, v[160:163] offset:49152
	ds_write_b128 v130, v[164:167] offset:57344
